# speedup vs baseline: 1.0390x; 1.0025x over previous
.LBB7_3:
	ds_read_b128 v[166:169], v162
	ds_read_b128 v[170:173], v162 offset:1024
	ds_read_b128 v[174:177], v162 offset:2048
	ds_read_b128 v[178:181], v162 offset:3072
	v_lshl_add_u64 v[230:231], v[136:137], 0, v[130:131]
	v_readfirstlane_b32 s9, v163
	v_lshl_add_u64 v[182:183], v[230:231], 0, s[16:17]
	s_mov_b32 m0, s9
	v_readfirstlane_b32 s9, v164
	global_load_lds_dwordx4 v[182:183], off
	v_lshl_add_u64 v[182:183], v[230:231], 0, s[18:19]
	s_mov_b32 m0, s9
	s_nop 0
	global_load_lds_dwordx4 v[182:183], off
	ds_read_b128 v[182:185], v141
	ds_read_b128 v[186:189], v141 offset:1024
	ds_read_b128 v[190:193], v140
	ds_read_b128 v[194:197], v140 offset:1024
	ds_read_b128 v[198:201], v139
	ds_read_b128 v[202:205], v139 offset:1024
	ds_read_b128 v[206:209], v138
	ds_read_b128 v[210:213], v138 offset:1024
	s_waitcnt lgkmcnt(8)
	s_barrier
	s_waitcnt lgkmcnt(0)
	s_setprio 1
	s_waitcnt lgkmcnt(0)
	v_mfma_f32_16x16x32_f16 v[126:129], v[182:185], v[166:169], v[126:129]
	v_mfma_f32_16x16x32_f16 v[122:125], v[182:185], v[174:177], v[122:125]
	v_mfma_f32_16x16x32_f16 v[118:121], v[190:193], v[166:169], v[118:121]
	v_mfma_f32_16x16x32_f16 v[114:117], v[190:193], v[174:177], v[114:117]
	v_mfma_f32_16x16x32_f16 v[110:113], v[198:201], v[166:169], v[110:113]
	v_mfma_f32_16x16x32_f16 v[106:109], v[198:201], v[174:177], v[106:109]
	v_mfma_f32_16x16x32_f16 v[102:105], v[206:209], v[166:169], v[102:105]
	v_mfma_f32_16x16x32_f16 v[98:101], v[206:209], v[174:177], v[98:101]
	s_setprio 0
	s_barrier
	v_lshl_add_u64 v[232:233], v[134:135], 0, v[130:131]
	v_readfirstlane_b32 s9, v145
	v_lshl_add_u64 v[234:235], v[232:233], 0, s[4:5]
	s_mov_b32 m0, s9
	v_readfirstlane_b32 s9, v146
	ds_read_b128 v[214:217], v160
	ds_read_b128 v[218:221], v160 offset:1024
	ds_read_b128 v[222:225], v160 offset:2048
	ds_read_b128 v[226:229], v160 offset:3072
	global_load_lds_dwordx4 v[234:235], off
	v_lshl_add_u64 v[234:235], v[232:233], 0, s[6:7]
	s_mov_b32 m0, s9
	s_nop 0
	global_load_lds_dwordx4 v[234:235], off
	s_barrier
	s_waitcnt lgkmcnt(0)
	s_setprio 1
	s_waitcnt lgkmcnt(0)
	v_mfma_f32_16x16x32_f16 v[126:129], v[186:189], v[170:173], v[126:129]
	v_mfma_f32_16x16x32_f16 v[122:125], v[186:189], v[178:181], v[122:125]
	v_mfma_f32_16x16x32_f16 v[118:121], v[194:197], v[170:173], v[118:121]
	v_mfma_f32_16x16x32_f16 v[114:117], v[194:197], v[178:181], v[114:117]
	v_mfma_f32_16x16x32_f16 v[110:113], v[202:205], v[170:173], v[110:113]
	v_mfma_f32_16x16x32_f16 v[106:109], v[202:205], v[178:181], v[106:109]
	v_mfma_f32_16x16x32_f16 v[102:105], v[210:213], v[170:173], v[102:105]
	v_mfma_f32_16x16x32_f16 v[98:101], v[210:213], v[178:181], v[98:101]
	s_setprio 0
	v_readfirstlane_b32 s9, v142
	v_lshl_add_u64 v[234:235], v[230:231], 0, s[4:5]
	s_mov_b32 m0, s9
	v_readfirstlane_b32 s9, v147
	s_barrier
	ds_read_b128 v[182:185], v141 offset:16384
	ds_read_b128 v[186:189], v141 offset:17408
	ds_read_b128 v[190:193], v140 offset:16384
	ds_read_b128 v[194:197], v140 offset:17408
	ds_read_b128 v[198:201], v139 offset:16384
	ds_read_b128 v[202:205], v139 offset:17408
	ds_read_b128 v[206:209], v138 offset:16384
	ds_read_b128 v[210:213], v138 offset:17408
	global_load_lds_dwordx4 v[234:235], off
	v_lshl_add_u64 v[234:235], v[230:231], 0, s[6:7]
	s_mov_b32 m0, s9
	s_nop 0
	global_load_lds_dwordx4 v[234:235], off
	s_barrier
	s_waitcnt lgkmcnt(0)
	s_setprio 1
	s_waitcnt lgkmcnt(0)
	v_mfma_f32_16x16x32_f16 v[30:33], v[182:185], v[214:217], v[30:33]
	v_mfma_f32_16x16x32_f16 v[26:29], v[182:185], v[222:225], v[26:29]
	v_mfma_f32_16x16x32_f16 v[22:25], v[190:193], v[214:217], v[22:25]
	v_mfma_f32_16x16x32_f16 v[18:21], v[190:193], v[222:225], v[18:21]
	v_mfma_f32_16x16x32_f16 v[14:17], v[198:201], v[214:217], v[14:17]
	v_mfma_f32_16x16x32_f16 v[10:13], v[198:201], v[222:225], v[10:13]
	v_mfma_f32_16x16x32_f16 v[6:9], v[206:209], v[214:217], v[6:9]
	v_mfma_f32_16x16x32_f16 v[2:5], v[206:209], v[222:225], v[2:5]
	s_setprio 0
	s_barrier
	v_readfirstlane_b32 s9, v150
	v_lshl_add_u64 v[166:167], v[232:233], 0, s[20:21]
	s_mov_b32 m0, s9
	v_readfirstlane_b32 s9, v152
	global_load_lds_dwordx4 v[166:167], off
	v_lshl_add_u64 v[166:167], v[232:233], 0, s[22:23]
	s_mov_b32 m0, s9
	s_nop 0
	global_load_lds_dwordx4 v[166:167], off
	s_waitcnt vmcnt(6)
	s_barrier
	s_setprio 1
	v_mfma_f32_16x16x32_f16 v[30:33], v[186:189], v[218:221], v[30:33]
	v_mfma_f32_16x16x32_f16 v[26:29], v[186:189], v[226:229], v[26:29]
	v_mfma_f32_16x16x32_f16 v[22:25], v[194:197], v[218:221], v[22:25]
	v_mfma_f32_16x16x32_f16 v[18:21], v[194:197], v[226:229], v[18:21]
	v_mfma_f32_16x16x32_f16 v[14:17], v[202:205], v[218:221], v[14:17]
	v_mfma_f32_16x16x32_f16 v[10:13], v[202:205], v[226:229], v[10:13]
	v_mfma_f32_16x16x32_f16 v[6:9], v[210:213], v[218:221], v[6:9]
	v_mfma_f32_16x16x32_f16 v[2:5], v[210:213], v[226:229], v[2:5]
	s_setprio 0
	s_barrier
	ds_read_b128 v[166:169], v151
	ds_read_b128 v[170:173], v151 offset:1024
	ds_read_b128 v[174:177], v151 offset:2048
	ds_read_b128 v[178:181], v151 offset:3072
	v_readfirstlane_b32 s9, v153
	v_lshl_add_u64 v[214:215], v[230:231], 0, s[20:21]
	s_mov_b32 m0, s9
	v_readfirstlane_b32 s9, v154
	ds_read_b128 v[182:185], v141 offset:32768
	ds_read_b128 v[186:189], v141 offset:33792
	ds_read_b128 v[190:193], v140 offset:32768
	ds_read_b128 v[194:197], v140 offset:33792
	ds_read_b128 v[198:201], v139 offset:32768
	ds_read_b128 v[202:205], v139 offset:33792
	ds_read_b128 v[206:209], v138 offset:32768
	ds_read_b128 v[210:213], v138 offset:33792
	global_load_lds_dwordx4 v[214:215], off
	v_lshl_add_u64 v[214:215], v[230:231], 0, s[22:23]
	s_mov_b32 m0, s9
	s_nop 0
	global_load_lds_dwordx4 v[214:215], off
	s_waitcnt lgkmcnt(8)
	s_barrier
	s_waitcnt lgkmcnt(0)
	s_setprio 1
	s_waitcnt lgkmcnt(0)
	v_mfma_f32_16x16x32_f16 v[126:129], v[182:185], v[166:169], v[126:129]
	v_mfma_f32_16x16x32_f16 v[122:125], v[182:185], v[174:177], v[122:125]
	v_mfma_f32_16x16x32_f16 v[118:121], v[190:193], v[166:169], v[118:121]
	v_mfma_f32_16x16x32_f16 v[114:117], v[190:193], v[174:177], v[114:117]
	v_mfma_f32_16x16x32_f16 v[110:113], v[198:201], v[166:169], v[110:113]
	v_mfma_f32_16x16x32_f16 v[106:109], v[198:201], v[174:177], v[106:109]
	v_mfma_f32_16x16x32_f16 v[102:105], v[206:209], v[166:169], v[102:105]
	v_mfma_f32_16x16x32_f16 v[98:101], v[206:209], v[174:177], v[98:101]
	s_setprio 0
	s_barrier
	v_readfirstlane_b32 s9, v155
	v_lshl_add_u64 v[234:235], v[232:233], 0, s[24:25]
	s_mov_b32 m0, s9
	v_readfirstlane_b32 s9, v156
	ds_read_b128 v[214:217], v144
	ds_read_b128 v[218:221], v144 offset:1024
	ds_read_b128 v[222:225], v144 offset:2048
	ds_read_b128 v[226:229], v144 offset:3072
	global_load_lds_dwordx4 v[234:235], off
	v_lshl_add_u64 v[234:235], v[232:233], 0, s[26:27]
	s_mov_b32 m0, s9
	s_nop 0
	global_load_lds_dwordx4 v[234:235], off
	s_barrier
	s_waitcnt lgkmcnt(0)
	s_setprio 1
	s_waitcnt lgkmcnt(0)
	v_mfma_f32_16x16x32_f16 v[126:129], v[186:189], v[170:173], v[126:129]
	v_mfma_f32_16x16x32_f16 v[122:125], v[186:189], v[178:181], v[122:125]
	v_mfma_f32_16x16x32_f16 v[118:121], v[194:197], v[170:173], v[118:121]
	v_mfma_f32_16x16x32_f16 v[114:117], v[194:197], v[178:181], v[114:117]
	v_mfma_f32_16x16x32_f16 v[110:113], v[202:205], v[170:173], v[110:113]
	v_mfma_f32_16x16x32_f16 v[106:109], v[202:205], v[178:181], v[106:109]
	v_mfma_f32_16x16x32_f16 v[102:105], v[210:213], v[170:173], v[102:105]
	v_mfma_f32_16x16x32_f16 v[98:101], v[210:213], v[178:181], v[98:101]
	s_setprio 0
	v_readfirstlane_b32 s9, v157
	v_lshl_add_u64 v[234:235], v[230:231], 0, s[24:25]
	s_mov_b32 m0, s9
	v_readfirstlane_b32 s9, v158
	s_barrier
	ds_read_b128 v[182:185], v141 offset:49152
	ds_read_b128 v[186:189], v141 offset:50176
	ds_read_b128 v[190:193], v140 offset:49152
	ds_read_b128 v[194:197], v140 offset:50176
	ds_read_b128 v[198:201], v139 offset:49152
	ds_read_b128 v[202:205], v139 offset:50176
	ds_read_b128 v[206:209], v138 offset:49152
	ds_read_b128 v[210:213], v138 offset:50176
	global_load_lds_dwordx4 v[234:235], off
	v_lshl_add_u64 v[230:231], v[230:231], 0, s[26:27]
	s_mov_b32 m0, s9
	s_nop 0
	global_load_lds_dwordx4 v[230:231], off
	s_barrier
	s_waitcnt lgkmcnt(0)
	s_setprio 1
	s_waitcnt lgkmcnt(0)
	v_mfma_f32_16x16x32_f16 v[30:33], v[182:185], v[214:217], v[30:33]
	v_mfma_f32_16x16x32_f16 v[26:29], v[182:185], v[222:225], v[26:29]
	v_mfma_f32_16x16x32_f16 v[22:25], v[190:193], v[214:217], v[22:25]
	v_mfma_f32_16x16x32_f16 v[18:21], v[190:193], v[222:225], v[18:21]
	v_mfma_f32_16x16x32_f16 v[14:17], v[198:201], v[214:217], v[14:17]
	v_mfma_f32_16x16x32_f16 v[10:13], v[198:201], v[222:225], v[10:13]
	v_mfma_f32_16x16x32_f16 v[6:9], v[206:209], v[214:217], v[6:9]
	v_mfma_f32_16x16x32_f16 v[2:5], v[206:209], v[222:225], v[2:5]
	s_setprio 0
	s_barrier
	v_readfirstlane_b32 s9, v159
	v_lshl_add_u64 v[166:167], v[232:233], 0, s[28:29]
	s_mov_b32 m0, s9
	v_readfirstlane_b32 s9, v161
	global_load_lds_dwordx4 v[166:167], off
	v_lshl_add_u64 v[166:167], v[232:233], 0, s[30:31]
	s_mov_b32 m0, s9
	s_nop 0
	global_load_lds_dwordx4 v[166:167], off
	s_waitcnt vmcnt(6)
	s_barrier
	s_setprio 1
	v_mfma_f32_16x16x32_f16 v[30:33], v[186:189], v[218:221], v[30:33]
	v_mfma_f32_16x16x32_f16 v[26:29], v[186:189], v[226:229], v[26:29]
	v_mfma_f32_16x16x32_f16 v[22:25], v[194:197], v[218:221], v[22:25]
	v_mfma_f32_16x16x32_f16 v[18:21], v[194:197], v[226:229], v[18:21]
	v_mfma_f32_16x16x32_f16 v[14:17], v[202:205], v[218:221], v[14:17]
	v_mfma_f32_16x16x32_f16 v[10:13], v[202:205], v[226:229], v[10:13]
	v_mfma_f32_16x16x32_f16 v[6:9], v[210:213], v[218:221], v[6:9]
	v_mfma_f32_16x16x32_f16 v[2:5], v[210:213], v[226:229], v[2:5]
	s_setprio 0
	s_add_i32 s3, s3, 2
	v_lshl_add_u64 v[134:135], v[134:135], 0, s[4:5]
	s_cmp_lt_u32 s3, 12
	v_lshl_add_u64 v[136:137], v[136:137], 0, s[4:5]
	s_barrier
	s_cbranch_scc1 .LBB7_3
	v_cmp_gt_u32_e32 vcc, 0x100, v0
	s_and_saveexec_b64 s[4:5], vcc
	s_cbranch_execz .Lop_deskew
	s_barrier
